# v33 + MoE gate/up unit set-up row-index loads batched + LayerNorm-1 router staging and MFMA loops with all loads of an iteration in flight
# speedup vs baseline: 1.0125x; 1.0055x over previous
.LBB0_1212:
	v_cmp_gt_u32_e32 vcc, s10, v4
	v_bfe_u32 v5, v4, 6, 5
	v_ashrrev_i32_e32 v192, 11, v4
	v_cndmask_b32_e32 v2, v244, v245, vcc
	v_lshl_add_u64 v[6:7], s[18:19], 0, v[2:3]
	v_lshlrev_b32_e32 v2, 11, v5
	v_lshl_add_u64 v[6:7], v[6:7], 0, v[2:3]
	v_lshlrev_b32_e32 v2, 1, v38
	v_lshl_add_u64 v[6:7], v[6:7], 0, v[2:3]
	global_load_dwordx4 v[124:127], v[6:7], off
	v_mad_i32_i24 v192, v192, s12, 0
	v_mul_u32_u24_e32 v5, 0x410, v5
	v_add3_u32 v192, v192, v5, v46
	v_add_u32_e32 v4, 0x200, v4
	v_cmp_gt_u32_e32 vcc, s10, v4
	v_bfe_u32 v5, v4, 6, 5
	v_ashrrev_i32_e32 v193, 11, v4
	v_cndmask_b32_e32 v2, v244, v245, vcc
	v_lshl_add_u64 v[6:7], s[18:19], 0, v[2:3]
	v_lshlrev_b32_e32 v2, 11, v5
	v_lshl_add_u64 v[6:7], v[6:7], 0, v[2:3]
	v_lshlrev_b32_e32 v2, 1, v38
	v_lshl_add_u64 v[6:7], v[6:7], 0, v[2:3]
	global_load_dwordx4 v[128:131], v[6:7], off
	v_mad_i32_i24 v193, v193, s12, 0
	v_mul_u32_u24_e32 v5, 0x410, v5
	v_add3_u32 v193, v193, v5, v46
	v_add_u32_e32 v4, 0x200, v4
	v_cmp_gt_u32_e32 vcc, s10, v4
	v_bfe_u32 v5, v4, 6, 5
	v_ashrrev_i32_e32 v194, 11, v4
	v_cndmask_b32_e32 v2, v244, v245, vcc
	v_lshl_add_u64 v[6:7], s[18:19], 0, v[2:3]
	v_lshlrev_b32_e32 v2, 11, v5
	v_lshl_add_u64 v[6:7], v[6:7], 0, v[2:3]
	v_lshlrev_b32_e32 v2, 1, v38
	v_lshl_add_u64 v[6:7], v[6:7], 0, v[2:3]
	global_load_dwordx4 v[132:135], v[6:7], off
	v_mad_i32_i24 v194, v194, s12, 0
	v_mul_u32_u24_e32 v5, 0x410, v5
	v_add3_u32 v194, v194, v5, v46
	v_add_u32_e32 v4, 0x200, v4
	v_cmp_gt_u32_e32 vcc, s10, v4
	v_bfe_u32 v5, v4, 6, 5
	v_ashrrev_i32_e32 v195, 11, v4
	v_cndmask_b32_e32 v2, v244, v245, vcc
	v_lshl_add_u64 v[6:7], s[18:19], 0, v[2:3]
	v_lshlrev_b32_e32 v2, 11, v5
	v_lshl_add_u64 v[6:7], v[6:7], 0, v[2:3]
	v_lshlrev_b32_e32 v2, 1, v38
	v_lshl_add_u64 v[6:7], v[6:7], 0, v[2:3]
	global_load_dwordx4 v[136:139], v[6:7], off
	v_mad_i32_i24 v195, v195, s12, 0
	v_mul_u32_u24_e32 v5, 0x410, v5
	v_add3_u32 v195, v195, v5, v46
	v_add_u32_e32 v4, 0x200, v4
	v_cmp_gt_u32_e32 vcc, s10, v4
	v_bfe_u32 v5, v4, 6, 5
	v_ashrrev_i32_e32 v196, 11, v4
	v_cndmask_b32_e32 v2, v244, v245, vcc
	v_lshl_add_u64 v[6:7], s[18:19], 0, v[2:3]
	v_lshlrev_b32_e32 v2, 11, v5
	v_lshl_add_u64 v[6:7], v[6:7], 0, v[2:3]
	v_lshlrev_b32_e32 v2, 1, v38
	v_lshl_add_u64 v[6:7], v[6:7], 0, v[2:3]
	global_load_dwordx4 v[140:143], v[6:7], off
	v_mad_i32_i24 v196, v196, s12, 0
	v_mul_u32_u24_e32 v5, 0x410, v5
	v_add3_u32 v196, v196, v5, v46
	v_add_u32_e32 v4, 0x200, v4
	v_cmp_gt_u32_e32 vcc, s10, v4
	v_bfe_u32 v5, v4, 6, 5
	v_ashrrev_i32_e32 v197, 11, v4
	v_cndmask_b32_e32 v2, v244, v245, vcc
	v_lshl_add_u64 v[6:7], s[18:19], 0, v[2:3]
	v_lshlrev_b32_e32 v2, 11, v5
	v_lshl_add_u64 v[6:7], v[6:7], 0, v[2:3]
	v_lshlrev_b32_e32 v2, 1, v38
	v_lshl_add_u64 v[6:7], v[6:7], 0, v[2:3]
	global_load_dwordx4 v[144:147], v[6:7], off
	v_mad_i32_i24 v197, v197, s12, 0
	v_mul_u32_u24_e32 v5, 0x410, v5
	v_add3_u32 v197, v197, v5, v46
	v_add_u32_e32 v4, 0x200, v4
	v_cmp_gt_u32_e32 vcc, s10, v4
	v_bfe_u32 v5, v4, 6, 5
	v_ashrrev_i32_e32 v198, 11, v4
	v_cndmask_b32_e32 v2, v244, v245, vcc
	v_lshl_add_u64 v[6:7], s[18:19], 0, v[2:3]
	v_lshlrev_b32_e32 v2, 11, v5
	v_lshl_add_u64 v[6:7], v[6:7], 0, v[2:3]
	v_lshlrev_b32_e32 v2, 1, v38
	v_lshl_add_u64 v[6:7], v[6:7], 0, v[2:3]
	global_load_dwordx4 v[148:151], v[6:7], off
	v_mad_i32_i24 v198, v198, s12, 0
	v_mul_u32_u24_e32 v5, 0x410, v5
	v_add3_u32 v198, v198, v5, v46
	v_add_u32_e32 v4, 0x200, v4
	v_cmp_gt_u32_e32 vcc, s10, v4
	v_bfe_u32 v5, v4, 6, 5
	v_ashrrev_i32_e32 v199, 11, v4
	v_cndmask_b32_e32 v2, v244, v245, vcc
	v_lshl_add_u64 v[6:7], s[18:19], 0, v[2:3]
	v_lshlrev_b32_e32 v2, 11, v5
	v_lshl_add_u64 v[6:7], v[6:7], 0, v[2:3]
	v_lshlrev_b32_e32 v2, 1, v38
	v_lshl_add_u64 v[6:7], v[6:7], 0, v[2:3]
	global_load_dwordx4 v[152:155], v[6:7], off
	v_mad_i32_i24 v199, v199, s12, 0
	v_mul_u32_u24_e32 v5, 0x410, v5
	v_add3_u32 v199, v199, v5, v46
	v_add_u32_e32 v4, 0x200, v4
	s_waitcnt vmcnt(7)
	ds_write_b128 v192, v[124:127]
	s_waitcnt vmcnt(6)
	ds_write_b128 v193, v[128:131]
	s_waitcnt vmcnt(5)
	ds_write_b128 v194, v[132:135]
	s_waitcnt vmcnt(4)
	ds_write_b128 v195, v[136:139]
	s_waitcnt vmcnt(3)
	ds_write_b128 v196, v[140:143]
	s_waitcnt vmcnt(2)
	ds_write_b128 v197, v[144:147]
	s_waitcnt vmcnt(1)
	ds_write_b128 v198, v[148:151]
	s_waitcnt vmcnt(0)
	ds_write_b128 v199, v[152:155]

.LBB0_1217:
	v_cmp_gt_u32_e32 vcc, s10, v22
	v_bfe_u32 v23, v22, 6, 5
	v_ashrrev_i32_e32 v192, 11, v22
	v_cndmask_b32_e32 v2, v244, v245, vcc
	v_lshl_add_u64 v[24:25], s[18:19], 0, v[2:3]
	v_lshlrev_b32_e32 v2, 11, v23
	v_lshl_add_u64 v[24:25], v[24:25], 0, v[2:3]
	v_lshlrev_b32_e32 v2, 1, v38
	v_lshl_add_u64 v[24:25], v[24:25], 0, v[2:3]
	global_load_dwordx4 v[124:127], v[24:25], off offset:1024
	v_mad_i32_i24 v192, v192, s12, 0
	v_mul_u32_u24_e32 v23, 0x410, v23
	v_add3_u32 v192, v192, v23, v46
	v_add_u32_e32 v22, 0x200, v22
	v_cmp_gt_u32_e32 vcc, s10, v22
	v_bfe_u32 v23, v22, 6, 5
	v_ashrrev_i32_e32 v193, 11, v22
	v_cndmask_b32_e32 v2, v244, v245, vcc
	v_lshl_add_u64 v[24:25], s[18:19], 0, v[2:3]
	v_lshlrev_b32_e32 v2, 11, v23
	v_lshl_add_u64 v[24:25], v[24:25], 0, v[2:3]
	v_lshlrev_b32_e32 v2, 1, v38
	v_lshl_add_u64 v[24:25], v[24:25], 0, v[2:3]
	global_load_dwordx4 v[128:131], v[24:25], off offset:1024
	v_mad_i32_i24 v193, v193, s12, 0
	v_mul_u32_u24_e32 v23, 0x410, v23
	v_add3_u32 v193, v193, v23, v46
	v_add_u32_e32 v22, 0x200, v22
	v_cmp_gt_u32_e32 vcc, s10, v22
	v_bfe_u32 v23, v22, 6, 5
	v_ashrrev_i32_e32 v194, 11, v22
	v_cndmask_b32_e32 v2, v244, v245, vcc
	v_lshl_add_u64 v[24:25], s[18:19], 0, v[2:3]
	v_lshlrev_b32_e32 v2, 11, v23
	v_lshl_add_u64 v[24:25], v[24:25], 0, v[2:3]
	v_lshlrev_b32_e32 v2, 1, v38
	v_lshl_add_u64 v[24:25], v[24:25], 0, v[2:3]
	global_load_dwordx4 v[132:135], v[24:25], off offset:1024
	v_mad_i32_i24 v194, v194, s12, 0
	v_mul_u32_u24_e32 v23, 0x410, v23
	v_add3_u32 v194, v194, v23, v46
	v_add_u32_e32 v22, 0x200, v22
	v_cmp_gt_u32_e32 vcc, s10, v22
	v_bfe_u32 v23, v22, 6, 5
	v_ashrrev_i32_e32 v195, 11, v22
	v_cndmask_b32_e32 v2, v244, v245, vcc
	v_lshl_add_u64 v[24:25], s[18:19], 0, v[2:3]
	v_lshlrev_b32_e32 v2, 11, v23
	v_lshl_add_u64 v[24:25], v[24:25], 0, v[2:3]
	v_lshlrev_b32_e32 v2, 1, v38
	v_lshl_add_u64 v[24:25], v[24:25], 0, v[2:3]
	global_load_dwordx4 v[136:139], v[24:25], off offset:1024
	v_mad_i32_i24 v195, v195, s12, 0
	v_mul_u32_u24_e32 v23, 0x410, v23
	v_add3_u32 v195, v195, v23, v46
	v_add_u32_e32 v22, 0x200, v22
	v_cmp_gt_u32_e32 vcc, s10, v22
	v_bfe_u32 v23, v22, 6, 5
	v_ashrrev_i32_e32 v196, 11, v22
	v_cndmask_b32_e32 v2, v244, v245, vcc
	v_lshl_add_u64 v[24:25], s[18:19], 0, v[2:3]
	v_lshlrev_b32_e32 v2, 11, v23
	v_lshl_add_u64 v[24:25], v[24:25], 0, v[2:3]
	v_lshlrev_b32_e32 v2, 1, v38
	v_lshl_add_u64 v[24:25], v[24:25], 0, v[2:3]
	global_load_dwordx4 v[140:143], v[24:25], off offset:1024
	v_mad_i32_i24 v196, v196, s12, 0
	v_mul_u32_u24_e32 v23, 0x410, v23
	v_add3_u32 v196, v196, v23, v46
	v_add_u32_e32 v22, 0x200, v22
	v_cmp_gt_u32_e32 vcc, s10, v22
	v_bfe_u32 v23, v22, 6, 5
	v_ashrrev_i32_e32 v197, 11, v22
	v_cndmask_b32_e32 v2, v244, v245, vcc
	v_lshl_add_u64 v[24:25], s[18:19], 0, v[2:3]
	v_lshlrev_b32_e32 v2, 11, v23
	v_lshl_add_u64 v[24:25], v[24:25], 0, v[2:3]
	v_lshlrev_b32_e32 v2, 1, v38
	v_lshl_add_u64 v[24:25], v[24:25], 0, v[2:3]
	global_load_dwordx4 v[144:147], v[24:25], off offset:1024
	v_mad_i32_i24 v197, v197, s12, 0
	v_mul_u32_u24_e32 v23, 0x410, v23
	v_add3_u32 v197, v197, v23, v46
	v_add_u32_e32 v22, 0x200, v22
	v_cmp_gt_u32_e32 vcc, s10, v22
	v_bfe_u32 v23, v22, 6, 5
	v_ashrrev_i32_e32 v198, 11, v22
	v_cndmask_b32_e32 v2, v244, v245, vcc
	v_lshl_add_u64 v[24:25], s[18:19], 0, v[2:3]
	v_lshlrev_b32_e32 v2, 11, v23
	v_lshl_add_u64 v[24:25], v[24:25], 0, v[2:3]
	v_lshlrev_b32_e32 v2, 1, v38
	v_lshl_add_u64 v[24:25], v[24:25], 0, v[2:3]
	global_load_dwordx4 v[148:151], v[24:25], off offset:1024
	v_mad_i32_i24 v198, v198, s12, 0
	v_mul_u32_u24_e32 v23, 0x410, v23
	v_add3_u32 v198, v198, v23, v46
	v_add_u32_e32 v22, 0x200, v22
	v_cmp_gt_u32_e32 vcc, s10, v22
	v_bfe_u32 v23, v22, 6, 5
	v_ashrrev_i32_e32 v199, 11, v22
	v_cndmask_b32_e32 v2, v244, v245, vcc
	v_lshl_add_u64 v[24:25], s[18:19], 0, v[2:3]
	v_lshlrev_b32_e32 v2, 11, v23
	v_lshl_add_u64 v[24:25], v[24:25], 0, v[2:3]
	v_lshlrev_b32_e32 v2, 1, v38
	v_lshl_add_u64 v[24:25], v[24:25], 0, v[2:3]
	global_load_dwordx4 v[152:155], v[24:25], off offset:1024
	v_mad_i32_i24 v199, v199, s12, 0
	v_mul_u32_u24_e32 v23, 0x410, v23
	v_add3_u32 v199, v199, v23, v46
	v_add_u32_e32 v22, 0x200, v22
	s_waitcnt vmcnt(7)
	ds_write_b128 v192, v[124:127]
	s_waitcnt vmcnt(6)
	ds_write_b128 v193, v[128:131]
	s_waitcnt vmcnt(5)
	ds_write_b128 v194, v[132:135]
	s_waitcnt vmcnt(4)
	ds_write_b128 v195, v[136:139]
	s_waitcnt vmcnt(3)
	ds_write_b128 v196, v[140:143]
	s_waitcnt vmcnt(2)
	ds_write_b128 v197, v[144:147]
	s_waitcnt vmcnt(1)
	ds_write_b128 v198, v[148:151]
	s_waitcnt vmcnt(0)
	ds_write_b128 v199, v[152:155]

.LBB0_1401:
	v_cndmask_b32_e64 v4, 0, 1, s[26:27]
	v_cmp_ne_u32_e64 s[2:3], 1, v4
	s_andn2_b64 vcc, exec, s[26:27]
	v_mov_b32_e32 v156, v146
	v_mov_b32_e32 v158, v148
	v_mov_b32_e32 v157, v2
	v_mov_b32_e32 v159, v150
	s_cbranch_vccnz .LBB0_1403
	v_lshl_add_u64 v[4:5], v[136:137], 2, s[16:17]
	global_load_dword v156, v[4:5], off
	global_load_dword v157, v[4:5], off offset:512
	v_lshl_add_u64 v[4:5], v[132:133], 2, s[16:17]
	global_load_dword v158, v[4:5], off
	global_load_dword v159, v[4:5], off offset:512
	s_waitcnt vmcnt(0)
	v_lshl_add_u32 v156, v156, 10, v1
	v_lshl_add_u32 v157, v157, 10, v1
	v_lshl_add_u32 v158, v158, 10, v143
	v_lshl_add_u32 v159, v159, 10, v143
